# stack10 = stack9 + QKV 1024-column K loop rewritten: weight-fragment loads spread between the MFMAs and re-requested two k-steps ahead right behind their last use, last trip peeled
# speedup vs baseline: 1.0116x; 1.0099x over previous
; #define REP(n) _Pragma("unroll 1") for (int rep_ = 0; rep_ < (n); ++rep_)
; #define LOADB(dst, ks_) do { const unsigned char* ub_ = wb + (size_t)((ks_) * 144) * 1024; \
;         _Pragma("unroll") for (int j_ = 0; j_ < 8; ++j_) dst[j_] = *(const bf16x8*)(ub_ + j_ * 1024 + voff); } while (0)
; #define LOADA(fd, ks_) do { _Pragma("unroll") for (int mi_ = 0; mi_ < 4; ++mi_) fd[mi_] = AFRAG(mi_, ks_); } while (0)
; #define LOADB(dst, ks_) do { const unsigned char* ub_ = wb + (size_t)((ks_) * 64) * 1024; \
;         _Pragma("unroll") for (int j_ = 0; j_ < 8; ++j_) dst[j_] = *(const bf16x8*)(ub_ + j_ * 1024 + voff); } while (0)
; #define LOADA(fd, ks_) do { _Pragma("unroll") for (int mi_ = 0; mi_ < 4; ++mi_) fd[mi_] = AFRAG(mi_, ks_); } while (0)
; DEVINL void phase2(const Params& P, unsigned char* smem, XPre& X, const bool have_pre) {
;     ...
;             f32x4 acc[8][4];
;             REP(P2_RK) {
; #pragma unroll
;             for (int i = 0; i < 8; ++i)
; #pragma unroll
;                 for (int mi = 0; mi < 4; ++mi) acc[i][mi] = (f32x4){0.f, 0.f, 0.f, 0.f};
;             if (!SKIPF(256)) {
;                 const unsigned char* wb = (const unsigned char*)(P.ws + WS_WQF) + (size_t)(64 * pass + 8 * wv) * 1024;
;                 bf16x8 b0[8], b1[8];
;     ...
;                 bf16x8 fa[4];
;                 LOADB(b0, 0); LOADA(fa, 0);
.LBB0_203:
	s_and_b64 vcc, exec, s[0:1]
	s_cbranch_vccz .LBB0_190
	s_mov_b32 s0, 0
	s_and_b64 vcc, exec, s[86:87]
	s_cbranch_vccz .LBB0_208
	s_lshl_b32 s1, s8, 6
	s_add_i32 s6, s1, s3
	s_ashr_i32 s7, s6, 31
	s_lshl_b64 s[6:7], s[6:7], 10
	v_lshl_add_u64 v[200:201], v[194:195], 0, s[6:7]
	v_add_co_u32_e32 v2, vcc, 0x1000, v200
	global_load_dwordx4 v[130:133], v[200:201], off
	global_load_dwordx4 v[134:137], v[200:201], off offset:1024
	global_load_dwordx4 v[138:141], v[200:201], off offset:2048
	global_load_dwordx4 v[142:145], v[200:201], off offset:3072
	v_addc_co_u32_e32 v3, vcc, 0, v201, vcc
	global_load_dwordx4 v[158:161], v[2:3], off
	global_load_dwordx4 v[154:157], v[2:3], off offset:1024
	global_load_dwordx4 v[150:153], v[2:3], off offset:2048
	global_load_dwordx4 v[146:149], v[2:3], off offset:3072
	s_waitcnt lgkmcnt(3)
	ds_read_b128 v[174:177], v213
	s_waitcnt lgkmcnt(3)
	ds_read_b128 v[170:173], v213 offset:32768
	s_waitcnt lgkmcnt(3)
	ds_read_b128 v[166:169], v214
	s_waitcnt lgkmcnt(3)
	ds_read_b128 v[162:165], v215
	v_mov_b32_e32 v2, 0
	v_lshl_add_u64 v[202:203], v[198:199], 0, s[6:7]
	v_mov_b32_e32 v178, v217
	v_mov_b32_e32 v3, v2
	v_mov_b32_e32 v4, v2
	v_mov_b32_e32 v5, v2
	v_mov_b32_e32 v18, v2
	v_mov_b32_e32 v19, v2
	v_mov_b32_e32 v20, v2
	v_mov_b32_e32 v21, v2
	v_mov_b32_e32 v34, v2
	v_mov_b32_e32 v35, v2
	v_mov_b32_e32 v36, v2
	v_mov_b32_e32 v37, v2
	v_mov_b32_e32 v50, v2
	v_mov_b32_e32 v51, v2
	v_mov_b32_e32 v52, v2
	v_mov_b32_e32 v53, v2
	v_mov_b32_e32 v10, v2
	v_mov_b32_e32 v11, v2
	v_mov_b32_e32 v12, v2
	v_mov_b32_e32 v13, v2
	v_mov_b32_e32 v22, v2
	v_mov_b32_e32 v23, v2
	v_mov_b32_e32 v24, v2
	v_mov_b32_e32 v25, v2
	v_mov_b32_e32 v38, v2
	v_mov_b32_e32 v39, v2
	v_mov_b32_e32 v40, v2
	v_mov_b32_e32 v41, v2
	v_mov_b32_e32 v54, v2
	v_mov_b32_e32 v55, v2
	v_mov_b32_e32 v56, v2
	v_mov_b32_e32 v57, v2
	v_mov_b32_e32 v14, v2
	v_mov_b32_e32 v15, v2
	v_mov_b32_e32 v16, v2
	v_mov_b32_e32 v17, v2
	v_mov_b32_e32 v30, v2
	v_mov_b32_e32 v31, v2
	v_mov_b32_e32 v32, v2
	v_mov_b32_e32 v33, v2
	v_mov_b32_e32 v46, v2
	v_mov_b32_e32 v47, v2
	v_mov_b32_e32 v48, v2
	v_mov_b32_e32 v49, v2
	v_mov_b32_e32 v62, v2
	v_mov_b32_e32 v63, v2
	v_mov_b32_e32 v64, v2
	v_mov_b32_e32 v65, v2
	v_mov_b32_e32 v70, v2
	v_mov_b32_e32 v71, v2
	v_mov_b32_e32 v72, v2
	v_mov_b32_e32 v73, v2
	v_mov_b32_e32 v86, v2
	v_mov_b32_e32 v87, v2
	v_mov_b32_e32 v88, v2
	v_mov_b32_e32 v89, v2
	v_mov_b32_e32 v106, v2
	v_mov_b32_e32 v107, v2
	v_mov_b32_e32 v108, v2
	v_mov_b32_e32 v109, v2
	v_mov_b32_e32 v122, v2
	v_mov_b32_e32 v123, v2
	v_mov_b32_e32 v124, v2
	v_mov_b32_e32 v125, v2
	v_mov_b32_e32 v66, v2
	v_mov_b32_e32 v67, v2
	v_mov_b32_e32 v68, v2
	v_mov_b32_e32 v69, v2
	v_mov_b32_e32 v82, v2
	v_mov_b32_e32 v83, v2
	v_mov_b32_e32 v84, v2
	v_mov_b32_e32 v85, v2
	v_mov_b32_e32 v98, v2
	v_mov_b32_e32 v99, v2
	v_mov_b32_e32 v100, v2
	v_mov_b32_e32 v101, v2
	v_mov_b32_e32 v114, v2
	v_mov_b32_e32 v115, v2
	v_mov_b32_e32 v116, v2
	v_mov_b32_e32 v117, v2
	v_mov_b32_e32 v74, v2
	v_mov_b32_e32 v75, v2
	v_mov_b32_e32 v76, v2
	v_mov_b32_e32 v77, v2
	v_mov_b32_e32 v90, v2
	v_mov_b32_e32 v91, v2
	v_mov_b32_e32 v92, v2
	v_mov_b32_e32 v93, v2
	v_mov_b32_e32 v102, v2
	v_mov_b32_e32 v103, v2
	v_mov_b32_e32 v104, v2
	v_mov_b32_e32 v105, v2
	v_mov_b32_e32 v118, v2
	v_mov_b32_e32 v119, v2
	v_mov_b32_e32 v120, v2
	v_mov_b32_e32 v121, v2
	v_mov_b32_e32 v78, v2
	v_mov_b32_e32 v79, v2
	v_mov_b32_e32 v80, v2
	v_mov_b32_e32 v81, v2
	v_mov_b32_e32 v94, v2
	v_mov_b32_e32 v95, v2
	v_mov_b32_e32 v96, v2
	v_mov_b32_e32 v97, v2
	v_mov_b32_e32 v110, v2
	v_mov_b32_e32 v111, v2
	v_mov_b32_e32 v112, v2
	v_mov_b32_e32 v113, v2
	v_mov_b32_e32 v126, v2
	v_mov_b32_e32 v127, v2
	v_mov_b32_e32 v128, v2
	v_mov_b32_e32 v129, v2
	v_mov_b32_e32 v58, v2
	v_mov_b32_e32 v59, v2
	v_mov_b32_e32 v60, v2
	v_mov_b32_e32 v61, v2
	v_mov_b32_e32 v42, v2
	v_mov_b32_e32 v43, v2
	v_mov_b32_e32 v44, v2
	v_mov_b32_e32 v45, v2
	v_mov_b32_e32 v26, v2
	v_mov_b32_e32 v27, v2
	v_mov_b32_e32 v28, v2
	v_mov_b32_e32 v29, v2
	v_mov_b32_e32 v6, v2
	v_mov_b32_e32 v7, v2
	v_mov_b32_e32 v8, v2
	v_mov_b32_e32 v9, v2
	s_mov_b64 s[6:7], 0x1000
	v_lshl_add_u64 v[202:203], v[202:203], 0, s[6:7]
	global_load_dwordx4 v[218:221], v[202:203], off offset:-4096
	global_load_dwordx4 v[222:225], v[202:203], off offset:-3072
	global_load_dwordx4 v[226:229], v[202:203], off offset:-2048
	global_load_dwordx4 v[230:233], v[202:203], off offset:-1024
	global_load_dwordx4 v[234:237], v[202:203], off
	global_load_dwordx4 v[238:241], v[202:203], off offset:1024
	global_load_dwordx4 v[242:245], v[202:203], off offset:2048
	global_load_dwordx4 v[246:249], v[202:203], off offset:3072
; #define LOADB(dst, ks_) do { const unsigned char* ub_ = wb + (size_t)((ks_) * 144) * 1024; \
;         _Pragma("unroll") for (int j_ = 0; j_ < 8; ++j_) dst[j_] = *(const bf16x8*)(ub_ + j_ * 1024 + voff); } while (0)
; #define LOADA(fd, ks_) do { _Pragma("unroll") for (int mi_ = 0; mi_ < 4; ++mi_) fd[mi_] = AFRAG(mi_, ks_); } while (0)
; #define MMA(src, fs, ksn_) do { _Pragma("unroll") for (int mi_ = 0; mi_ < 4; ++mi_) { \
;         _Pragma("unroll") for (int j_ = 0; j_ < 8; ++j_) acc[j_][mi_] = __builtin_amdgcn_mfma_f32_16x16x32_bf16(src[j_], fs[mi_], acc[j_][mi_], 0, 0, 0); \
;         fs[mi_] = AFRAG(mi_, (ksn_) < 32 ? (ksn_) : 31); } } while (0)
; #define LOADB(dst, ks_) do { const unsigned char* ub_ = wb + (size_t)((ks_) * 64) * 1024; \
;         _Pragma("unroll") for (int j_ = 0; j_ < 8; ++j_) dst[j_] = *(const bf16x8*)(ub_ + j_ * 1024 + voff); } while (0)
; #define LOADA(fd, ks_) do { _Pragma("unroll") for (int mi_ = 0; mi_ < 4; ++mi_) fd[mi_] = AFRAG(mi_, ks_); } while (0)
; #define MMA(src, fs, ksn_) do { _Pragma("unroll") for (int mi_ = 0; mi_ < 4; ++mi_) { \
;         _Pragma("unroll") for (int j_ = 0; j_ < 8; ++j_) acc[j_][mi_] = __builtin_amdgcn_mfma_f32_16x16x32_bf16(src[j_], fs[mi_], acc[j_][mi_], 0, 0, 0); \
;         fs[mi_] = AFRAG(mi_, (ksn_) < 32 ? (ksn_) : 31); } } while (0)
; DEVINL void phase2(const Params& P, unsigned char* smem, XPre& X, const bool have_pre) {
;     ...
;                 bf16x8 fa[4];
;                 LOADB(b0, 0); LOADA(fa, 0);
; #pragma unroll 1
;                 for (int ks = 0; ks < 32; ks += 2) {
;                     LOADB(b1, ks + 1);
;                     __builtin_amdgcn_sched_barrier(0);
;                     MMA(b0, fa, ks + 1);
;                     __builtin_amdgcn_sched_barrier(0);
;                     LOADB(b0, ks + 2 < 32 ? ks + 2 : 31);
;                     __builtin_amdgcn_sched_barrier(0);
;                     MMA(b1, fa, ks + 2);
;                     __builtin_amdgcn_sched_barrier(0);
;                 }
.LBB0_206:
	s_add_i32 s1, s0, 2
	s_mul_i32 s18, s1, 0x24000
	s_add_i32 s18, s18, 0x1000
	v_xor_b32_e32 v252, v178, v181
	v_lshl_add_u32 v252, v252, 4, v212
	v_add_u32_e32 v253, 0x10000, v252
	v_lshl_add_u64 v[250:251], v[200:201], 0, s[18:19]
	s_waitcnt vmcnt(15) lgkmcnt(3)
	v_mfma_f32_16x16x32_bf16 v[126:129], v[130:133], v[174:177], v[126:129]
	s_waitcnt lgkmcnt(2)
	v_mfma_f32_16x16x32_bf16 v[110:113], v[130:133], v[170:173], v[110:113]
	s_waitcnt vmcnt(14)
	v_mfma_f32_16x16x32_bf16 v[118:121], v[134:137], v[174:177], v[118:121]
	v_mfma_f32_16x16x32_bf16 v[102:105], v[134:137], v[170:173], v[102:105]
	s_waitcnt vmcnt(13)
	v_mfma_f32_16x16x32_bf16 v[114:117], v[138:141], v[174:177], v[114:117]
	v_mfma_f32_16x16x32_bf16 v[98:101], v[138:141], v[170:173], v[98:101]
	s_waitcnt vmcnt(12)
	v_mfma_f32_16x16x32_bf16 v[122:125], v[142:145], v[174:177], v[122:125]
	v_mfma_f32_16x16x32_bf16 v[106:109], v[142:145], v[170:173], v[106:109]
	s_waitcnt vmcnt(11)
	v_mfma_f32_16x16x32_bf16 v[62:65], v[158:161], v[174:177], v[62:65]
	v_mfma_f32_16x16x32_bf16 v[46:49], v[158:161], v[170:173], v[46:49]
	s_waitcnt vmcnt(10)
	v_mfma_f32_16x16x32_bf16 v[54:57], v[154:157], v[174:177], v[54:57]
	v_mfma_f32_16x16x32_bf16 v[38:41], v[154:157], v[170:173], v[38:41]
	s_waitcnt vmcnt(9)
	v_mfma_f32_16x16x32_bf16 v[50:53], v[150:153], v[174:177], v[50:53]
	v_mfma_f32_16x16x32_bf16 v[34:37], v[150:153], v[170:173], v[34:37]
	s_waitcnt vmcnt(8)
	v_mfma_f32_16x16x32_bf16 v[58:61], v[146:149], v[174:177], v[58:61]
	v_mfma_f32_16x16x32_bf16 v[42:45], v[146:149], v[170:173], v[42:45]
	s_waitcnt lgkmcnt(1)
	v_mfma_f32_16x16x32_bf16 v[94:97], v[130:133], v[166:169], v[94:97]
	s_waitcnt lgkmcnt(0)
	v_mfma_f32_16x16x32_bf16 v[78:81], v[130:133], v[162:165], v[78:81]
	global_load_dwordx4 v[130:133], v[250:251], off offset:-4096
	v_mfma_f32_16x16x32_bf16 v[90:93], v[134:137], v[166:169], v[90:93]
	v_mfma_f32_16x16x32_bf16 v[74:77], v[134:137], v[162:165], v[74:77]
	global_load_dwordx4 v[134:137], v[250:251], off offset:-3072
	ds_read_b128 v[174:177], v252
	v_mfma_f32_16x16x32_bf16 v[82:85], v[138:141], v[166:169], v[82:85]
	v_mfma_f32_16x16x32_bf16 v[66:69], v[138:141], v[162:165], v[66:69]
	global_load_dwordx4 v[138:141], v[250:251], off offset:-2048
	ds_read_b128 v[170:173], v252 offset:32768
	v_mfma_f32_16x16x32_bf16 v[86:89], v[142:145], v[166:169], v[86:89]
	v_mfma_f32_16x16x32_bf16 v[70:73], v[142:145], v[162:165], v[70:73]
	global_load_dwordx4 v[142:145], v[250:251], off offset:-1024
	v_mfma_f32_16x16x32_bf16 v[30:33], v[158:161], v[166:169], v[30:33]
	v_mfma_f32_16x16x32_bf16 v[14:17], v[158:161], v[162:165], v[14:17]
	global_load_dwordx4 v[158:161], v[250:251], off
	v_mfma_f32_16x16x32_bf16 v[22:25], v[154:157], v[166:169], v[22:25]
	v_mfma_f32_16x16x32_bf16 v[10:13], v[154:157], v[162:165], v[10:13]
	global_load_dwordx4 v[154:157], v[250:251], off offset:1024
	v_mfma_f32_16x16x32_bf16 v[18:21], v[150:153], v[166:169], v[18:21]
	v_mfma_f32_16x16x32_bf16 v[2:5], v[150:153], v[162:165], v[2:5]
	global_load_dwordx4 v[150:153], v[250:251], off offset:2048
	v_mfma_f32_16x16x32_bf16 v[26:29], v[146:149], v[166:169], v[26:29]
	v_mfma_f32_16x16x32_bf16 v[6:9], v[146:149], v[162:165], v[6:9]
	global_load_dwordx4 v[146:149], v[250:251], off offset:3072
	ds_read_b128 v[166:169], v253
	ds_read_b128 v[162:165], v253 offset:32768
	s_mov_b64 s[6:7], 0x48000
	v_lshl_add_u32 v252, s1, 2, v211
	v_lshl_add_u64 v[202:203], v[202:203], 0, s[6:7]
	v_xor_b32_e32 v252, v252, v181
	v_lshl_add_u32 v252, v252, 4, v212
	v_add_u32_e32 v253, 0x10000, v252
	s_waitcnt vmcnt(15) lgkmcnt(3)
	v_mfma_f32_16x16x32_bf16 v[126:129], v[218:221], v[174:177], v[126:129]
	s_waitcnt lgkmcnt(2)
	v_mfma_f32_16x16x32_bf16 v[110:113], v[218:221], v[170:173], v[110:113]
	s_waitcnt vmcnt(14)
	v_mfma_f32_16x16x32_bf16 v[118:121], v[222:225], v[174:177], v[118:121]
	v_mfma_f32_16x16x32_bf16 v[102:105], v[222:225], v[170:173], v[102:105]
	s_waitcnt vmcnt(13)
	v_mfma_f32_16x16x32_bf16 v[114:117], v[226:229], v[174:177], v[114:117]
	v_mfma_f32_16x16x32_bf16 v[98:101], v[226:229], v[170:173], v[98:101]
	s_waitcnt vmcnt(12)
	v_mfma_f32_16x16x32_bf16 v[122:125], v[230:233], v[174:177], v[122:125]
	v_mfma_f32_16x16x32_bf16 v[106:109], v[230:233], v[170:173], v[106:109]
	s_waitcnt vmcnt(11)
	v_mfma_f32_16x16x32_bf16 v[62:65], v[234:237], v[174:177], v[62:65]
	v_mfma_f32_16x16x32_bf16 v[46:49], v[234:237], v[170:173], v[46:49]
	s_waitcnt vmcnt(10)
	v_mfma_f32_16x16x32_bf16 v[54:57], v[238:241], v[174:177], v[54:57]
	v_mfma_f32_16x16x32_bf16 v[38:41], v[238:241], v[170:173], v[38:41]
	s_waitcnt vmcnt(9)
	v_mfma_f32_16x16x32_bf16 v[50:53], v[242:245], v[174:177], v[50:53]
	v_mfma_f32_16x16x32_bf16 v[34:37], v[242:245], v[170:173], v[34:37]
	s_waitcnt vmcnt(8)
	v_mfma_f32_16x16x32_bf16 v[58:61], v[246:249], v[174:177], v[58:61]
	v_mfma_f32_16x16x32_bf16 v[42:45], v[246:249], v[170:173], v[42:45]
	s_waitcnt lgkmcnt(1)
	v_mfma_f32_16x16x32_bf16 v[94:97], v[218:221], v[166:169], v[94:97]
	s_waitcnt lgkmcnt(0)
	v_mfma_f32_16x16x32_bf16 v[78:81], v[218:221], v[162:165], v[78:81]
	global_load_dwordx4 v[218:221], v[202:203], off offset:-4096
	v_mfma_f32_16x16x32_bf16 v[90:93], v[222:225], v[166:169], v[90:93]
	v_mfma_f32_16x16x32_bf16 v[74:77], v[222:225], v[162:165], v[74:77]
	global_load_dwordx4 v[222:225], v[202:203], off offset:-3072
	ds_read_b128 v[174:177], v252
	v_mfma_f32_16x16x32_bf16 v[82:85], v[226:229], v[166:169], v[82:85]
	v_mfma_f32_16x16x32_bf16 v[66:69], v[226:229], v[162:165], v[66:69]
	global_load_dwordx4 v[226:229], v[202:203], off offset:-2048
	ds_read_b128 v[170:173], v252 offset:32768
	v_mfma_f32_16x16x32_bf16 v[86:89], v[230:233], v[166:169], v[86:89]
	v_mfma_f32_16x16x32_bf16 v[70:73], v[230:233], v[162:165], v[70:73]
	global_load_dwordx4 v[230:233], v[202:203], off offset:-1024
	v_mfma_f32_16x16x32_bf16 v[30:33], v[234:237], v[166:169], v[30:33]
	v_mfma_f32_16x16x32_bf16 v[14:17], v[234:237], v[162:165], v[14:17]
	global_load_dwordx4 v[234:237], v[202:203], off
	v_mfma_f32_16x16x32_bf16 v[22:25], v[238:241], v[166:169], v[22:25]
	v_mfma_f32_16x16x32_bf16 v[10:13], v[238:241], v[162:165], v[10:13]
	global_load_dwordx4 v[238:241], v[202:203], off offset:1024
	v_mfma_f32_16x16x32_bf16 v[18:21], v[242:245], v[166:169], v[18:21]
	v_mfma_f32_16x16x32_bf16 v[2:5], v[242:245], v[162:165], v[2:5]
	global_load_dwordx4 v[242:245], v[202:203], off offset:2048
	v_mfma_f32_16x16x32_bf16 v[26:29], v[246:249], v[166:169], v[26:29]
	v_mfma_f32_16x16x32_bf16 v[6:9], v[246:249], v[162:165], v[6:9]
	global_load_dwordx4 v[246:249], v[202:203], off offset:3072
	ds_read_b128 v[166:169], v253
	ds_read_b128 v[162:165], v253 offset:32768
	v_add_u32_e32 v178, 8, v178
	s_mov_b32 s0, s1
	s_cmp_lt_u32 s0, 30
	s_cbranch_scc1 .LBB0_206
; #define LOADB(dst, ks_) do { const unsigned char* ub_ = wb + (size_t)((ks_) * 144) * 1024; \
;         _Pragma("unroll") for (int j_ = 0; j_ < 8; ++j_) dst[j_] = *(const bf16x8*)(ub_ + j_ * 1024 + voff); } while (0)
; #define LOADA(fd, ks_) do { _Pragma("unroll") for (int mi_ = 0; mi_ < 4; ++mi_) fd[mi_] = AFRAG(mi_, ks_); } while (0)
; #define MMA(src, fs, ksn_) do { _Pragma("unroll") for (int mi_ = 0; mi_ < 4; ++mi_) { \
;         _Pragma("unroll") for (int j_ = 0; j_ < 8; ++j_) acc[j_][mi_] = __builtin_amdgcn_mfma_f32_16x16x32_bf16(src[j_], fs[mi_], acc[j_][mi_], 0, 0, 0); \
;         fs[mi_] = AFRAG(mi_, (ksn_) < 32 ? (ksn_) : 31); } } while (0)
; #define LOADB(dst, ks_) do { const unsigned char* ub_ = wb + (size_t)((ks_) * 64) * 1024; \
;         _Pragma("unroll") for (int j_ = 0; j_ < 8; ++j_) dst[j_] = *(const bf16x8*)(ub_ + j_ * 1024 + voff); } while (0)
; #define LOADA(fd, ks_) do { _Pragma("unroll") for (int mi_ = 0; mi_ < 4; ++mi_) fd[mi_] = AFRAG(mi_, ks_); } while (0)
; #define MMA(src, fs, ksn_) do { _Pragma("unroll") for (int mi_ = 0; mi_ < 4; ++mi_) { \
;         _Pragma("unroll") for (int j_ = 0; j_ < 8; ++j_) acc[j_][mi_] = __builtin_amdgcn_mfma_f32_16x16x32_bf16(src[j_], fs[mi_], acc[j_][mi_], 0, 0, 0); \
;         fs[mi_] = AFRAG(mi_, (ksn_) < 32 ? (ksn_) : 31); } } while (0)
; DEVINL void phase2(const Params& P, unsigned char* smem, XPre& X, const bool have_pre) {
;     ...
;                 bf16x8 fa[4];
;                 LOADB(b0, 0); LOADA(fa, 0);
; #pragma unroll 1
;                 for (int ks = 0; ks < 32; ks += 2) {
;                     LOADB(b1, ks + 1);
;                     __builtin_amdgcn_sched_barrier(0);
;                     MMA(b0, fa, ks + 1);
;                     __builtin_amdgcn_sched_barrier(0);
;                     LOADB(b0, ks + 2 < 32 ? ks + 2 : 31);
;                     __builtin_amdgcn_sched_barrier(0);
;                     MMA(b1, fa, ks + 2);
;                     __builtin_amdgcn_sched_barrier(0);
;                 }
	v_xor_b32_e32 v252, v178, v181
	v_lshl_add_u32 v252, v252, 4, v212
	v_add_u32_e32 v253, 0x10000, v252
	s_waitcnt vmcnt(15) lgkmcnt(3)
	v_mfma_f32_16x16x32_bf16 v[126:129], v[130:133], v[174:177], v[126:129]
	s_waitcnt lgkmcnt(2)
	v_mfma_f32_16x16x32_bf16 v[110:113], v[130:133], v[170:173], v[110:113]
	s_waitcnt vmcnt(14)
	v_mfma_f32_16x16x32_bf16 v[118:121], v[134:137], v[174:177], v[118:121]
	v_mfma_f32_16x16x32_bf16 v[102:105], v[134:137], v[170:173], v[102:105]
	s_waitcnt vmcnt(13)
	v_mfma_f32_16x16x32_bf16 v[114:117], v[138:141], v[174:177], v[114:117]
	v_mfma_f32_16x16x32_bf16 v[98:101], v[138:141], v[170:173], v[98:101]
	s_waitcnt vmcnt(12)
	v_mfma_f32_16x16x32_bf16 v[122:125], v[142:145], v[174:177], v[122:125]
	v_mfma_f32_16x16x32_bf16 v[106:109], v[142:145], v[170:173], v[106:109]
	s_waitcnt vmcnt(11)
	v_mfma_f32_16x16x32_bf16 v[62:65], v[158:161], v[174:177], v[62:65]
	v_mfma_f32_16x16x32_bf16 v[46:49], v[158:161], v[170:173], v[46:49]
	s_waitcnt vmcnt(10)
	v_mfma_f32_16x16x32_bf16 v[54:57], v[154:157], v[174:177], v[54:57]
	v_mfma_f32_16x16x32_bf16 v[38:41], v[154:157], v[170:173], v[38:41]
	s_waitcnt vmcnt(9)
	v_mfma_f32_16x16x32_bf16 v[50:53], v[150:153], v[174:177], v[50:53]
	v_mfma_f32_16x16x32_bf16 v[34:37], v[150:153], v[170:173], v[34:37]
	s_waitcnt vmcnt(8)
	v_mfma_f32_16x16x32_bf16 v[58:61], v[146:149], v[174:177], v[58:61]
	v_mfma_f32_16x16x32_bf16 v[42:45], v[146:149], v[170:173], v[42:45]
	s_waitcnt lgkmcnt(1)
	v_mfma_f32_16x16x32_bf16 v[94:97], v[130:133], v[166:169], v[94:97]
	s_waitcnt lgkmcnt(0)
	v_mfma_f32_16x16x32_bf16 v[78:81], v[130:133], v[162:165], v[78:81]
	v_mfma_f32_16x16x32_bf16 v[90:93], v[134:137], v[166:169], v[90:93]
	v_mfma_f32_16x16x32_bf16 v[74:77], v[134:137], v[162:165], v[74:77]
	ds_read_b128 v[174:177], v252
	v_mfma_f32_16x16x32_bf16 v[82:85], v[138:141], v[166:169], v[82:85]
	v_mfma_f32_16x16x32_bf16 v[66:69], v[138:141], v[162:165], v[66:69]
	ds_read_b128 v[170:173], v252 offset:32768
	v_mfma_f32_16x16x32_bf16 v[86:89], v[142:145], v[166:169], v[86:89]
	v_mfma_f32_16x16x32_bf16 v[70:73], v[142:145], v[162:165], v[70:73]
	v_mfma_f32_16x16x32_bf16 v[30:33], v[158:161], v[166:169], v[30:33]
	v_mfma_f32_16x16x32_bf16 v[14:17], v[158:161], v[162:165], v[14:17]
	v_mfma_f32_16x16x32_bf16 v[22:25], v[154:157], v[166:169], v[22:25]
	v_mfma_f32_16x16x32_bf16 v[10:13], v[154:157], v[162:165], v[10:13]
	v_mfma_f32_16x16x32_bf16 v[18:21], v[150:153], v[166:169], v[18:21]
	v_mfma_f32_16x16x32_bf16 v[2:5], v[150:153], v[162:165], v[2:5]
	v_mfma_f32_16x16x32_bf16 v[26:29], v[146:149], v[166:169], v[26:29]
	v_mfma_f32_16x16x32_bf16 v[6:9], v[146:149], v[162:165], v[6:9]
	ds_read_b128 v[166:169], v253
	ds_read_b128 v[162:165], v253 offset:32768
	s_waitcnt vmcnt(7) lgkmcnt(3)
	v_mfma_f32_16x16x32_bf16 v[126:129], v[218:221], v[174:177], v[126:129]
	s_waitcnt lgkmcnt(2)
	v_mfma_f32_16x16x32_bf16 v[110:113], v[218:221], v[170:173], v[110:113]
	s_waitcnt vmcnt(6)
	v_mfma_f32_16x16x32_bf16 v[118:121], v[222:225], v[174:177], v[118:121]
	v_mfma_f32_16x16x32_bf16 v[102:105], v[222:225], v[170:173], v[102:105]
	s_waitcnt vmcnt(5)
	v_mfma_f32_16x16x32_bf16 v[114:117], v[226:229], v[174:177], v[114:117]
	v_mfma_f32_16x16x32_bf16 v[98:101], v[226:229], v[170:173], v[98:101]
	s_waitcnt vmcnt(4)
	v_mfma_f32_16x16x32_bf16 v[122:125], v[230:233], v[174:177], v[122:125]
	v_mfma_f32_16x16x32_bf16 v[106:109], v[230:233], v[170:173], v[106:109]
	s_waitcnt vmcnt(3)
	v_mfma_f32_16x16x32_bf16 v[62:65], v[234:237], v[174:177], v[62:65]
	v_mfma_f32_16x16x32_bf16 v[46:49], v[234:237], v[170:173], v[46:49]
	s_waitcnt vmcnt(2)
	v_mfma_f32_16x16x32_bf16 v[54:57], v[238:241], v[174:177], v[54:57]
	v_mfma_f32_16x16x32_bf16 v[38:41], v[238:241], v[170:173], v[38:41]
	s_waitcnt vmcnt(1)
	v_mfma_f32_16x16x32_bf16 v[50:53], v[242:245], v[174:177], v[50:53]
	v_mfma_f32_16x16x32_bf16 v[34:37], v[242:245], v[170:173], v[34:37]
	s_waitcnt vmcnt(0)
	v_mfma_f32_16x16x32_bf16 v[58:61], v[246:249], v[174:177], v[58:61]
	v_mfma_f32_16x16x32_bf16 v[42:45], v[246:249], v[170:173], v[42:45]
	s_waitcnt lgkmcnt(1)
	v_mfma_f32_16x16x32_bf16 v[94:97], v[218:221], v[166:169], v[94:97]
	s_waitcnt lgkmcnt(0)
	v_mfma_f32_16x16x32_bf16 v[78:81], v[218:221], v[162:165], v[78:81]
	v_mfma_f32_16x16x32_bf16 v[90:93], v[222:225], v[166:169], v[90:93]
	v_mfma_f32_16x16x32_bf16 v[74:77], v[222:225], v[162:165], v[74:77]
	v_mfma_f32_16x16x32_bf16 v[82:85], v[226:229], v[166:169], v[82:85]
	v_mfma_f32_16x16x32_bf16 v[66:69], v[226:229], v[162:165], v[66:69]
	v_mfma_f32_16x16x32_bf16 v[86:89], v[230:233], v[166:169], v[86:89]
	v_mfma_f32_16x16x32_bf16 v[70:73], v[230:233], v[162:165], v[70:73]
	v_mfma_f32_16x16x32_bf16 v[30:33], v[234:237], v[166:169], v[30:33]
	v_mfma_f32_16x16x32_bf16 v[14:17], v[234:237], v[162:165], v[14:17]
	v_mfma_f32_16x16x32_bf16 v[22:25], v[238:241], v[166:169], v[22:25]
	v_mfma_f32_16x16x32_bf16 v[10:13], v[238:241], v[162:165], v[10:13]
	v_mfma_f32_16x16x32_bf16 v[18:21], v[242:245], v[166:169], v[18:21]
	v_mfma_f32_16x16x32_bf16 v[2:5], v[242:245], v[162:165], v[2:5]
	v_mfma_f32_16x16x32_bf16 v[26:29], v[246:249], v[166:169], v[26:29]
	v_mfma_f32_16x16x32_bf16 v[6:9], v[246:249], v[162:165], v[6:9]
	s_and_b64 vcc, exec, s[88:89]
	s_cbranch_vccz .LBB0_190
	s_branch .LBB0_209
